# P7/P8 grouped GEMMs: per-unit scheduler step (next unit index, group-size division, LDS tile->expert lookup) computed one unit early inside the previous epilogue's load-wait window; unit header only c
# baseline (speedup 1.0000x reference)
.LBB0_975:
	s_andn2_b64 vcc, exec, s[4:5]
	s_mov_b32 s34, s10
	s_mov_b32 s96, s55
	s_mov_b32 s10, s79
	s_mov_b32 s55, s78
	s_mov_b64 s[38:39], s[30:31]
	s_mov_b64 s[36:37], s[28:29]
	s_cbranch_vccz .LBB0_997
	s_mov_b32 s78, s98
	s_mov_b32 s79, s99
	s_mov_b64 s[28:29], s[100:101]
	s_not_b64 s[4:5], s[36:37]
	s_branch .LBB0_979

.LBB0_994:
	s_ashr_i32 s36, s34, 3
	s_lshl_b32 s2, s34, 7
	s_ashr_i32 s37, s36, 31
	v_readlane_b32 s80, v239, 7
	s_and_b32 s2, s2, 0x380
	s_lshl_b64 s[36:37], s[36:37], 13
	v_readlane_b32 s86, v239, 13
	v_or_b32_e32 v2, s2, v219
	v_readlane_b32 s87, v239, 14
	s_add_u32 s36, s86, s36
	s_waitcnt vmcnt(0)
	s_addc_u32 s37, s87, s37
	v_lshlrev_b32_e32 v4, 2, v2
	v_mov_b32_e32 v5, v199
	global_load_dwordx4 v[26:29], v4, s[36:37]
	global_load_dwordx4 v[30:33], v4, s[36:37] offset:16
	v_lshl_add_u64 v[4:5], s[36:37], 0, v[4:5]
	s_mov_b64 s[36:37], 0x1000
	s_movk_i32 s2, 0x1000
	v_lshl_add_u64 v[6:7], v[4:5], 0, s[36:37]
	v_add_co_u32_e32 v4, vcc, s2, v4
	v_mov_b32_e32 v8, v186
	s_nop 0
	v_addc_co_u32_e32 v5, vcc, 0, v5, vcc
	global_load_dwordx4 v[34:37], v[4:5], off
	global_load_dwordx4 v[38:41], v[6:7], off offset:16
	s_mov_b64 s[100:101], 0
	s_and_b64 vcc, exec, s[28:29]
	s_cbranch_vccz .Lhh7_done
	s_add_i32 s2, s67, 3
	s_mul_i32 s2, s2, s50
	s_add_i32 s2, s2, s9
	s_cmp_ge_i32 s2, s53
	s_cbranch_scc1 .Lhh7_done
	s_ashr_i32 s11, s2, 31
	s_lshr_b32 s11, s11, 27
	s_add_i32 s11, s2, s11
	s_ashr_i32 s32, s11, 5
	s_lshl_b32 s32, s32, 2
	s_sub_i32 s47, s51, s32
	s_min_i32 s47, s47, 4
	s_abs_i32 s48, s47
	v_cvt_f32_u32_e32 v244, s48
	s_sub_i32 s44, 0, s48
	s_andn2_b32 s11, s11, 31
	s_sub_i32 s2, s2, s11
	v_rcp_iflag_f32_e32 v244, v244
	s_add_i32 s11, s32, s8
	s_abs_i32 s32, s2
	s_xor_b32 s49, s2, s47
	v_mul_f32_e32 v244, 0x4f7ffffe, v244
	v_cvt_u32_f32_e32 v244, v244
	s_ashr_i32 s49, s49, 31
	v_readfirstlane_b32 s45, v244
	s_mul_i32 s44, s44, s45
	s_mul_hi_u32 s44, s45, s44
	s_add_i32 s45, s45, s44
	s_mul_hi_u32 s44, s32, s45
	s_mul_i32 s45, s44, s48
	s_sub_i32 s32, s32, s45
	s_add_i32 s46, s44, 1
	s_sub_i32 s45, s32, s48
	s_cmp_ge_u32 s32, s48
	s_cselect_b32 s44, s46, s44
	s_cselect_b32 s32, s45, s32
	s_add_i32 s45, s44, 1
	s_cmp_ge_u32 s32, s48
	s_cselect_b32 s32, s45, s44
	s_xor_b32 s32, s32, s49
	s_sub_i32 s32, s32, s49
	s_mul_i32 s47, s32, s47
	s_sub_i32 s2, s2, s47
	s_add_i32 s98, s11, s2
	s_lshl_b32 s2, s98, 2
	s_add_i32 s2, s2, 0
	s_add_i32 s2, s2, 0x21400
	v_mov_b32_e32 v244, s2
	ds_read_b32 v244, v244
	s_waitcnt lgkmcnt(0)
	v_readfirstlane_b32 s2, v244
	s_lshl_b32 s2, s2, 3
	s_add_i32 s99, s2, s32
	s_mov_b64 s[100:101], -1
.Lhh7_done:
	v_mov_b32_e32 v6, v190
	v_mov_b32_e32 v14, v178
	v_mov_b32_e32 v24, v183
	v_mov_b32_e32 v20, v192
	v_lshl_add_u32 v4, s96, 8, v218
	v_ashrrev_i32_e32 v5, 31, v4
	v_lshlrev_b64 v[4:5], 10, v[4:5]
	v_mov_b32_e32 v3, v199
	v_mov_b32_e32 v12, v182
	v_mov_b32_e32 v42, v179
	v_mov_b32_e32 v22, v188
	v_lshl_add_u64 v[4:5], s[58:59], 0, v[4:5]
	v_lshl_add_u64 v[2:3], v[4:5], 0, v[2:3]
	v_lshl_add_u64 v[2:3], v[2:3], 0, v[204:205]
	s_mov_b32 s2, 0x8000
	v_readlane_b32 s81, v239, 8
	v_readlane_b32 s82, v239, 9
	v_readlane_b32 s83, v239, 10
	v_readlane_b32 s84, v239, 11
	v_readlane_b32 s85, v239, 12
	v_readlane_b32 s88, v239, 15
	v_readlane_b32 s89, v239, 16
	v_readlane_b32 s90, v239, 17
	v_readlane_b32 s91, v239, 18
	v_readlane_b32 s92, v239, 19
	v_readlane_b32 s93, v239, 20
	v_readlane_b32 s94, v239, 21
	v_readlane_b32 s95, v239, 22
	s_waitcnt vmcnt(0)
	v_mov_b32_e32 v7, v26
	v_mov_b32_e32 v9, v30
	v_pk_mul_f32 v[16:17], v[8:9], s[24:25]
	v_mov_b32_e32 v26, v191
	v_sub_f32_e32 v16, v16, v17
	v_mov_b32_e32 v21, v28
	v_pk_mul_f32 v[10:11], v[26:27], s[24:25]
	v_max_f32_e32 v16, 0xc1898193, v16
	v_pk_mul_f32 v[18:19], v[6:7], s[24:25]
	v_pk_mul_f32 v[6:7], v[20:21], s[24:25]
	v_add_f32_e32 v25, 1.0, v35
	v_add_f32_e32 v15, 1.0, v38
	v_sub_f32_e32 v10, v10, v11
	v_pk_mul_f32 v[20:21], v[14:15], s[26:27]
	v_pk_mul_f32 v[14:15], v[24:25], s[26:27]
	v_exp_f32_e32 v25, v16
	v_max_f32_e32 v10, 0xc1898193, v10
	v_sub_f32_e32 v18, v18, v19
	v_sub_f32_e32 v6, v6, v7
	v_exp_f32_e32 v26, v10
	v_sub_f32_e32 v14, v14, v15
	v_max_f32_e32 v18, 0xc1898193, v18
	v_max_f32_e32 v6, 0xc1898193, v6
	v_med3_f32 v14, v14, s71, v223
	v_mov_b32_e32 v30, v187
	v_mov_b32_e32 v23, v32
	v_add_f32_e32 v13, 1.0, v34
	v_add_f32_e32 v43, 1.0, v39
	v_exp_f32_e32 v24, v18
	v_sub_f32_e32 v20, v20, v21
	v_exp_f32_e32 v28, v6
	v_mul_f32_e32 v10, v10, v14
	v_add_f32_e32 v14, 1.0, v25
	v_pk_mul_f32 v[8:9], v[30:31], s[24:25]
	v_pk_mul_f32 v[4:5], v[22:23], s[24:25]
	v_pk_mul_f32 v[22:23], v[12:13], s[26:27]
	v_pk_mul_f32 v[12:13], v[42:43], s[26:27]
	v_med3_f32 v20, v20, s71, v223
	v_rcp_f32_e32 v14, v14
	v_sub_f32_e32 v8, v8, v9
	v_sub_f32_e32 v12, v12, v13
	v_mul_f32_e32 v16, v16, v20
	v_add_f32_e32 v20, 1.0, v26
	v_max_f32_e32 v8, 0xc1898193, v8
	v_med3_f32 v12, v12, s71, v223
	v_rcp_f32_e32 v20, v20
	v_exp_f32_e32 v27, v8
	v_mul_f32_e32 v8, v8, v12
	v_add_f32_e32 v12, 1.0, v24
	v_add_f32_e32 v24, 1.0, v28
	v_mul_f32_e32 v14, v14, v16
	v_rcp_f32_e32 v16, v24
	v_add_f32_e32 v25, 1.0, v36
	v_mov_b32_e32 v24, v184
	v_sub_f32_e32 v22, v22, v23
	v_pk_mul_f32 v[24:25], v[24:25], s[26:27]
	v_sub_f32_e32 v4, v4, v5
	v_med3_f32 v22, v22, s71, v223
	v_mul_f32_e32 v10, v20, v10
	v_sub_f32_e32 v20, v24, v25
	v_max_f32_e32 v4, 0xc1898193, v4
	v_mul_f32_e32 v18, v18, v22
	v_add_f32_e32 v22, 1.0, v27
	v_med3_f32 v20, v20, s71, v223
	v_add_f32_e32 v27, 1.0, v40
	v_mov_b32_e32 v26, v180
	v_exp_f32_e32 v30, v4
	v_rcp_f32_e32 v12, v12
	v_mul_f32_e32 v6, v6, v20
	v_pk_mul_f32 v[26:27], v[26:27], s[26:27]
	v_rcp_f32_e32 v22, v22
	v_mul_f32_e32 v6, v16, v6
	v_sub_f32_e32 v16, v26, v27
	v_mov_b32_e32 v28, v193
	v_med3_f32 v16, v16, s71, v223
	v_pk_mul_f32 v[28:29], v[28:29], s[24:25]
	v_mul_f32_e32 v4, v4, v16
	v_sub_f32_e32 v16, v28, v29
	v_mov_b32_e32 v32, v189
	v_mul_f32_e32 v12, v12, v18
	v_add_f32_e32 v18, 1.0, v30
	v_max_f32_e32 v16, 0xc1898193, v16
	v_pk_mul_f32 v[30:31], v[32:33], s[24:25]
	v_mul_f32_e32 v8, v22, v8
	v_rcp_f32_e32 v18, v18
	v_sub_f32_e32 v20, v30, v31
	v_exp_f32_e32 v22, v16
	v_max_f32_e32 v20, 0xc1898193, v20
	v_exp_f32_e32 v24, v20
	v_mul_f32_e32 v4, v18, v4
	v_add_f32_e32 v18, 1.0, v22
	v_add_f32_e32 v33, 1.0, v37
	v_mov_b32_e32 v32, v185
	v_rcp_f32_e32 v18, v18
	v_pk_mul_f32 v[32:33], v[32:33], s[26:27]
	v_mov_b32_e32 v36, v199
	v_add_f32_e32 v22, 1.0, v24
	v_sub_f32_e32 v24, v32, v33
	v_cvt_pk_fp8_f32 v36, v12, v10
	v_med3_f32 v24, v24, s71, v223
	v_mul_f32_e32 v16, v16, v24
	v_mul_f32_e32 v16, v18, v16
	v_add_f32_e32 v35, 1.0, v41
	v_mov_b32_e32 v34, v181
	v_cvt_pk_fp8_f32 v36, v6, v16 op_sel:[0,0,1]
	v_fma_f32 v6, v174, s24, -v19
	v_rcp_f32_e32 v22, v22
	v_pk_mul_f32 v[34:35], v[34:35], s[26:27]
	v_mov_b32_e32 v37, v199
	v_max_f32_e32 v6, 0xc1898193, v6
	v_sub_f32_e32 v18, v34, v35
	v_cvt_pk_fp8_f32 v37, v14, v8
	v_exp_f32_e32 v12, v6
	v_med3_f32 v10, v18, s71, v223
	v_mul_f32_e32 v10, v20, v10
	v_mul_f32_e32 v10, v22, v10
	v_cvt_pk_fp8_f32 v37, v4, v10 op_sel:[0,0,1]
	v_add_f32_e32 v4, 1.0, v12
	v_rcp_f32_e32 v4, v4
	v_fma_f32 v8, v170, s24, -v17
	v_fma_f32 v12, v166, s26, -v23
	v_max_f32_e32 v8, 0xc1898193, v8
	v_med3_f32 v12, v12, s71, v223
	v_exp_f32_e32 v14, v8
	v_mul_f32_e32 v6, v6, v12
	v_mul_f32_e32 v4, v4, v6
	v_fma_f32 v6, v162, s26, -v21
	v_med3_f32 v6, v6, s71, v223
	v_mul_f32_e32 v6, v8, v6
	v_fma_f32 v8, v175, s24, -v11
	v_add_f32_e32 v10, 1.0, v14
	v_max_f32_e32 v8, 0xc1898193, v8
	v_rcp_f32_e32 v10, v10
	v_fma_f32 v12, v171, s24, -v9
	v_exp_f32_e32 v14, v8
	v_max_f32_e32 v12, 0xc1898193, v12
	v_exp_f32_e32 v16, v12
	v_mul_f32_e32 v6, v10, v6
	v_add_f32_e32 v10, 1.0, v14
	v_rcp_f32_e32 v10, v10
	v_add_f32_e32 v14, 1.0, v16
	v_fma_f32 v16, v167, s26, -v15
	v_med3_f32 v16, v16, s71, v223
	v_mul_f32_e32 v8, v8, v16
	v_mul_f32_e32 v8, v10, v8
	v_fma_f32 v10, v163, s26, -v13
	v_med3_f32 v10, v10, s71, v223
	v_mul_f32_e32 v10, v12, v10
	v_fma_f32 v12, v176, s24, -v7
	v_max_f32_e32 v12, 0xc1898193, v12
	v_rcp_f32_e32 v14, v14
	v_fma_f32 v16, v172, s24, -v5
	v_exp_f32_e32 v18, v12
	v_max_f32_e32 v16, 0xc1898193, v16
	v_exp_f32_e32 v20, v16
	v_mul_f32_e32 v10, v14, v10
	v_add_f32_e32 v14, 1.0, v18
	v_rcp_f32_e32 v14, v14
	v_add_f32_e32 v18, 1.0, v20
	v_fma_f32 v20, v168, s26, -v25
	v_med3_f32 v20, v20, s71, v223
	v_mul_f32_e32 v12, v12, v20
	v_mul_f32_e32 v12, v14, v12
	v_fma_f32 v14, v164, s26, -v27
	v_med3_f32 v14, v14, s71, v223
	v_mul_f32_e32 v14, v16, v14
	v_fma_f32 v16, v177, s24, -v29
	v_max_f32_e32 v16, 0xc1898193, v16
	v_rcp_f32_e32 v18, v18
	v_fma_f32 v20, v173, s24, -v31
	v_exp_f32_e32 v22, v16
	v_max_f32_e32 v20, 0xc1898193, v20
	v_exp_f32_e32 v24, v20
	v_mul_f32_e32 v14, v18, v14
	v_add_f32_e32 v18, 1.0, v22
	v_rcp_f32_e32 v18, v18
	v_add_f32_e32 v22, 1.0, v24
	v_fma_f32 v24, v169, s26, -v33
	v_med3_f32 v24, v24, s71, v223
	v_rcp_f32_e32 v22, v22
	v_mul_f32_e32 v16, v16, v24
	v_mov_b32_e32 v39, v199
	v_mul_f32_e32 v16, v18, v16
	v_fma_f32 v18, v165, s26, -v35
	v_cvt_pk_fp8_f32 v39, v6, v10
	v_med3_f32 v18, v18, s71, v223
	v_mov_b32_e32 v38, v199
	v_cvt_pk_fp8_f32 v38, v4, v8
	v_mul_f32_e32 v4, v20, v18
	v_mul_f32_e32 v4, v22, v4
	v_cvt_pk_fp8_f32 v39, v14, v4 op_sel:[0,0,1]
	v_fma_f32 v4, v158, s24, -v19
	v_max_f32_e32 v4, 0xc1898193, v4
	v_exp_f32_e32 v8, v4
	v_cvt_pk_fp8_f32 v38, v12, v16 op_sel:[0,0,1]
	v_fma_f32 v6, v154, s24, -v17
	v_fma_f32 v12, v150, s26, -v23
	v_add_f32_e32 v8, 1.0, v8
	v_rcp_f32_e32 v8, v8
	v_max_f32_e32 v6, 0xc1898193, v6
	v_med3_f32 v12, v12, s71, v223
	v_exp_f32_e32 v10, v6
	v_mul_f32_e32 v4, v4, v12
	v_mul_f32_e32 v4, v8, v4
	v_fma_f32 v8, v146, s26, -v21
	v_med3_f32 v8, v8, s71, v223
	v_mul_f32_e32 v6, v6, v8
	v_fma_f32 v8, v159, s24, -v11
	v_add_f32_e32 v10, 1.0, v10
	v_max_f32_e32 v8, 0xc1898193, v8
	v_rcp_f32_e32 v10, v10
	v_fma_f32 v12, v155, s24, -v9
	v_exp_f32_e32 v14, v8
	v_max_f32_e32 v12, 0xc1898193, v12
	v_exp_f32_e32 v16, v12
	v_mul_f32_e32 v6, v10, v6
	v_add_f32_e32 v10, 1.0, v14
	v_rcp_f32_e32 v10, v10
	v_add_f32_e32 v14, 1.0, v16
	v_fma_f32 v16, v151, s26, -v15
	v_med3_f32 v16, v16, s71, v223
	v_mul_f32_e32 v8, v8, v16
	v_mul_f32_e32 v8, v10, v8
	v_fma_f32 v10, v147, s26, -v13
	v_med3_f32 v10, v10, s71, v223
	v_mul_f32_e32 v10, v12, v10
	v_fma_f32 v12, v160, s24, -v7
	v_max_f32_e32 v12, 0xc1898193, v12
	v_rcp_f32_e32 v14, v14
	v_fma_f32 v16, v156, s24, -v5
	v_exp_f32_e32 v18, v12
	v_max_f32_e32 v16, 0xc1898193, v16
	v_exp_f32_e32 v20, v16
	v_mul_f32_e32 v10, v14, v10
	v_add_f32_e32 v14, 1.0, v18
	v_rcp_f32_e32 v14, v14
	v_add_f32_e32 v18, 1.0, v20
	v_fma_f32 v20, v152, s26, -v25
	v_med3_f32 v20, v20, s71, v223
	v_mul_f32_e32 v12, v12, v20
	v_mul_f32_e32 v12, v14, v12
	v_fma_f32 v14, v148, s26, -v27
	v_med3_f32 v14, v14, s71, v223
	v_mul_f32_e32 v14, v16, v14
	v_fma_f32 v16, v161, s24, -v29
	v_max_f32_e32 v16, 0xc1898193, v16
	v_rcp_f32_e32 v18, v18
	v_fma_f32 v20, v157, s24, -v31
	v_exp_f32_e32 v22, v16
	v_max_f32_e32 v20, 0xc1898193, v20
	v_exp_f32_e32 v24, v20
	v_mul_f32_e32 v14, v18, v14
	v_add_f32_e32 v18, 1.0, v22
	v_permlane16_swap_b32_e32 v36, v38
	v_permlane16_swap_b32_e32 v37, v39
	v_rcp_f32_e32 v18, v18
	global_store_dwordx4 v[2:3], v[36:39], off
	v_add_f32_e32 v22, 1.0, v24
	v_fma_f32 v24, v153, s26, -v33
	v_mov_b32_e32 v36, v199
	v_mov_b32_e32 v37, v199
	v_med3_f32 v24, v24, s71, v223
	v_cvt_pk_fp8_f32 v36, v4, v8
	v_cvt_pk_fp8_f32 v37, v6, v10
	v_fma_f32 v6, v142, s24, -v19
	v_rcp_f32_e32 v22, v22
	v_mul_f32_e32 v16, v16, v24
	v_max_f32_e32 v6, 0xc1898193, v6
	v_mul_f32_e32 v16, v18, v16
	v_fma_f32 v18, v149, s26, -v35
	v_fma_f32 v8, v138, s24, -v17
	v_exp_f32_e32 v10, v6
	v_med3_f32 v4, v18, s71, v223
	v_max_f32_e32 v8, 0xc1898193, v8
	v_mul_f32_e32 v4, v20, v4
	v_cvt_pk_fp8_f32 v36, v12, v16 op_sel:[0,0,1]
	v_exp_f32_e32 v12, v8
	v_mul_f32_e32 v4, v22, v4
	v_cvt_pk_fp8_f32 v37, v14, v4 op_sel:[0,0,1]
	v_add_f32_e32 v4, 1.0, v10
	v_rcp_f32_e32 v4, v4
	v_add_f32_e32 v10, 1.0, v12
	v_fma_f32 v12, v134, s26, -v23
	v_med3_f32 v12, v12, s71, v223
	v_mul_f32_e32 v6, v6, v12
	v_mul_f32_e32 v4, v4, v6
	v_fma_f32 v6, v130, s26, -v21
	v_med3_f32 v6, v6, s71, v223
	v_mul_f32_e32 v6, v8, v6
	v_fma_f32 v8, v143, s24, -v11
	v_max_f32_e32 v8, 0xc1898193, v8
	v_rcp_f32_e32 v10, v10
	v_fma_f32 v12, v139, s24, -v9
	v_exp_f32_e32 v14, v8
	v_max_f32_e32 v12, 0xc1898193, v12
	v_exp_f32_e32 v16, v12
	v_mul_f32_e32 v6, v10, v6
	v_add_f32_e32 v10, 1.0, v14
	v_rcp_f32_e32 v10, v10
	v_add_f32_e32 v14, 1.0, v16
	v_fma_f32 v16, v135, s26, -v15
	v_med3_f32 v16, v16, s71, v223
	v_mul_f32_e32 v8, v8, v16
	v_mul_f32_e32 v8, v10, v8
	v_fma_f32 v10, v131, s26, -v13
	v_med3_f32 v10, v10, s71, v223
	v_mul_f32_e32 v10, v12, v10
	v_fma_f32 v12, v144, s24, -v7
	v_max_f32_e32 v12, 0xc1898193, v12
	v_rcp_f32_e32 v14, v14
	v_fma_f32 v16, v140, s24, -v5
	v_exp_f32_e32 v18, v12
	v_max_f32_e32 v16, 0xc1898193, v16
	v_exp_f32_e32 v20, v16
	v_mul_f32_e32 v10, v14, v10
	v_add_f32_e32 v14, 1.0, v18
	v_rcp_f32_e32 v14, v14
	v_add_f32_e32 v18, 1.0, v20
	v_fma_f32 v20, v136, s26, -v25
	v_med3_f32 v20, v20, s71, v223
	v_mul_f32_e32 v12, v12, v20
	v_mul_f32_e32 v12, v14, v12
	v_fma_f32 v14, v132, s26, -v27
	v_med3_f32 v14, v14, s71, v223
	v_mul_f32_e32 v14, v16, v14
	v_fma_f32 v16, v145, s24, -v29
	v_max_f32_e32 v16, 0xc1898193, v16
	v_rcp_f32_e32 v18, v18
	v_fma_f32 v20, v141, s24, -v31
	v_exp_f32_e32 v22, v16
	v_max_f32_e32 v20, 0xc1898193, v20
	v_exp_f32_e32 v24, v20
	v_mul_f32_e32 v14, v18, v14
	v_add_f32_e32 v18, 1.0, v22
	v_rcp_f32_e32 v18, v18
	v_add_f32_e32 v22, 1.0, v24
	v_fma_f32 v24, v137, s26, -v33
	v_med3_f32 v24, v24, s71, v223
	v_rcp_f32_e32 v22, v22
	v_mul_f32_e32 v16, v16, v24
	v_mov_b32_e32 v39, v199
	v_mul_f32_e32 v16, v18, v16
	v_fma_f32 v18, v133, s26, -v35
	v_cvt_pk_fp8_f32 v39, v6, v10
	v_med3_f32 v18, v18, s71, v223
	v_mov_b32_e32 v38, v199
	v_cvt_pk_fp8_f32 v38, v4, v8
	v_mul_f32_e32 v4, v20, v18
	v_mul_f32_e32 v4, v22, v4
	v_cvt_pk_fp8_f32 v39, v14, v4 op_sel:[0,0,1]
	v_fma_f32 v4, v126, s24, -v19
	v_max_f32_e32 v4, 0xc1898193, v4
	v_exp_f32_e32 v8, v4
	v_cvt_pk_fp8_f32 v38, v12, v16 op_sel:[0,0,1]
	v_fma_f32 v6, v122, s24, -v17
	v_fma_f32 v12, v118, s26, -v23
	v_add_f32_e32 v8, 1.0, v8
	v_rcp_f32_e32 v8, v8
	v_max_f32_e32 v6, 0xc1898193, v6
	v_med3_f32 v12, v12, s71, v223
	v_exp_f32_e32 v10, v6
	v_mul_f32_e32 v4, v4, v12
	v_mul_f32_e32 v4, v8, v4
	v_fma_f32 v8, v114, s26, -v21
	v_med3_f32 v8, v8, s71, v223
	v_mul_f32_e32 v6, v6, v8
	v_fma_f32 v8, v127, s24, -v11
	v_add_f32_e32 v10, 1.0, v10
	v_max_f32_e32 v8, 0xc1898193, v8
	v_rcp_f32_e32 v10, v10
	v_fma_f32 v12, v123, s24, -v9
	v_exp_f32_e32 v14, v8
	v_max_f32_e32 v12, 0xc1898193, v12
	v_exp_f32_e32 v16, v12
	v_mul_f32_e32 v6, v10, v6
	v_add_f32_e32 v10, 1.0, v14
	v_rcp_f32_e32 v10, v10
	v_add_f32_e32 v14, 1.0, v16
	v_fma_f32 v16, v119, s26, -v15
	v_med3_f32 v16, v16, s71, v223
	v_mul_f32_e32 v8, v8, v16
	v_mul_f32_e32 v8, v10, v8
	v_fma_f32 v10, v115, s26, -v13
	v_med3_f32 v10, v10, s71, v223
	v_mul_f32_e32 v10, v12, v10
	v_fma_f32 v12, v128, s24, -v7
	v_max_f32_e32 v12, 0xc1898193, v12
	v_rcp_f32_e32 v14, v14
	v_fma_f32 v16, v124, s24, -v5
	v_exp_f32_e32 v18, v12
	v_max_f32_e32 v16, 0xc1898193, v16
	v_exp_f32_e32 v20, v16
	v_mul_f32_e32 v10, v14, v10
	v_add_f32_e32 v14, 1.0, v18
	v_rcp_f32_e32 v14, v14
	v_add_f32_e32 v18, 1.0, v20
	v_fma_f32 v20, v120, s26, -v25
	v_med3_f32 v20, v20, s71, v223
	v_mul_f32_e32 v12, v12, v20
	v_mul_f32_e32 v12, v14, v12
	v_fma_f32 v14, v116, s26, -v27
	v_med3_f32 v14, v14, s71, v223
	v_mul_f32_e32 v14, v16, v14
	v_fma_f32 v16, v129, s24, -v29
	v_max_f32_e32 v16, 0xc1898193, v16
	v_rcp_f32_e32 v18, v18
	v_fma_f32 v20, v125, s24, -v31
	v_exp_f32_e32 v22, v16
	v_max_f32_e32 v20, 0xc1898193, v20
	v_exp_f32_e32 v24, v20
	v_add_co_u32_e32 v40, vcc, s2, v2
	v_mul_f32_e32 v14, v18, v14
	v_add_f32_e32 v18, 1.0, v22
	v_permlane16_swap_b32_e32 v36, v38
	v_permlane16_swap_b32_e32 v37, v39
	v_addc_co_u32_e32 v41, vcc, 0, v3, vcc
	v_rcp_f32_e32 v18, v18
	global_store_dwordx4 v[40:41], v[36:39], off
	v_add_f32_e32 v22, 1.0, v24
	v_fma_f32 v24, v121, s26, -v33
	v_mov_b32_e32 v36, v199
	v_mov_b32_e32 v37, v199
	v_med3_f32 v24, v24, s71, v223
	v_cvt_pk_fp8_f32 v36, v4, v8
	v_cvt_pk_fp8_f32 v37, v6, v10
	v_fma_f32 v6, v110, s24, -v19
	v_rcp_f32_e32 v22, v22
	v_mul_f32_e32 v16, v16, v24
	v_max_f32_e32 v6, 0xc1898193, v6
	v_mul_f32_e32 v16, v18, v16
	v_fma_f32 v18, v117, s26, -v35
	v_fma_f32 v8, v106, s24, -v17
	v_exp_f32_e32 v10, v6
	v_med3_f32 v4, v18, s71, v223
	v_max_f32_e32 v8, 0xc1898193, v8
	v_mul_f32_e32 v4, v20, v4
	v_cvt_pk_fp8_f32 v36, v12, v16 op_sel:[0,0,1]
	v_exp_f32_e32 v12, v8
	v_mul_f32_e32 v4, v22, v4
	v_cvt_pk_fp8_f32 v37, v14, v4 op_sel:[0,0,1]
	v_add_f32_e32 v4, 1.0, v10
	v_rcp_f32_e32 v4, v4
	v_add_f32_e32 v10, 1.0, v12
	v_fma_f32 v12, v102, s26, -v23
	v_med3_f32 v12, v12, s71, v223
	v_mul_f32_e32 v6, v6, v12
	v_mul_f32_e32 v4, v4, v6
	v_fma_f32 v6, v90, s26, -v21
	v_med3_f32 v6, v6, s71, v223
	v_mul_f32_e32 v6, v8, v6
	v_fma_f32 v8, v111, s24, -v11
	v_max_f32_e32 v8, 0xc1898193, v8
	v_rcp_f32_e32 v10, v10
	v_fma_f32 v12, v107, s24, -v9
	v_exp_f32_e32 v14, v8
	v_max_f32_e32 v12, 0xc1898193, v12
	v_exp_f32_e32 v16, v12
	v_mul_f32_e32 v6, v10, v6
	v_add_f32_e32 v10, 1.0, v14
	v_rcp_f32_e32 v10, v10
	v_add_f32_e32 v14, 1.0, v16
	v_fma_f32 v16, v103, s26, -v15
	v_med3_f32 v16, v16, s71, v223
	v_mul_f32_e32 v8, v8, v16
	v_mul_f32_e32 v8, v10, v8
	v_fma_f32 v10, v91, s26, -v13
	v_med3_f32 v10, v10, s71, v223
	v_mul_f32_e32 v10, v12, v10
	v_fma_f32 v12, v112, s24, -v7
	v_max_f32_e32 v12, 0xc1898193, v12
	v_rcp_f32_e32 v14, v14
	v_fma_f32 v16, v108, s24, -v5
	v_exp_f32_e32 v18, v12
	v_max_f32_e32 v16, 0xc1898193, v16
	v_exp_f32_e32 v20, v16
	v_mul_f32_e32 v10, v14, v10
	v_add_f32_e32 v14, 1.0, v18
	v_rcp_f32_e32 v14, v14
	v_add_f32_e32 v18, 1.0, v20
	v_fma_f32 v20, v104, s26, -v25
	v_med3_f32 v20, v20, s71, v223
	v_mul_f32_e32 v12, v12, v20
	v_mul_f32_e32 v12, v14, v12
	v_fma_f32 v14, v92, s26, -v27
	v_med3_f32 v14, v14, s71, v223
	v_mul_f32_e32 v14, v16, v14
	v_fma_f32 v16, v113, s24, -v29
	v_max_f32_e32 v16, 0xc1898193, v16
	v_rcp_f32_e32 v18, v18
	v_fma_f32 v20, v109, s24, -v31
	v_exp_f32_e32 v22, v16
	v_max_f32_e32 v20, 0xc1898193, v20
	v_exp_f32_e32 v24, v20
	v_mul_f32_e32 v14, v18, v14
	v_add_f32_e32 v18, 1.0, v22
	v_rcp_f32_e32 v18, v18
	v_add_f32_e32 v22, 1.0, v24
	v_fma_f32 v24, v105, s26, -v33
	v_med3_f32 v24, v24, s71, v223
	v_rcp_f32_e32 v22, v22
	v_mul_f32_e32 v16, v16, v24
	v_mov_b32_e32 v39, v199
	v_mul_f32_e32 v16, v18, v16
	v_fma_f32 v18, v93, s26, -v35
	v_cvt_pk_fp8_f32 v39, v6, v10
	v_med3_f32 v18, v18, s71, v223
	v_mov_b32_e32 v38, v199
	v_cvt_pk_fp8_f32 v38, v4, v8
	v_mul_f32_e32 v4, v20, v18
	v_mul_f32_e32 v4, v22, v4
	v_cvt_pk_fp8_f32 v39, v14, v4 op_sel:[0,0,1]
	v_fma_f32 v4, v86, s24, -v19
	v_max_f32_e32 v4, 0xc1898193, v4
	v_exp_f32_e32 v8, v4
	v_cvt_pk_fp8_f32 v38, v12, v16 op_sel:[0,0,1]
	v_fma_f32 v6, v82, s24, -v17
	v_fma_f32 v12, v94, s26, -v23
	v_add_f32_e32 v8, 1.0, v8
	v_rcp_f32_e32 v8, v8
	v_max_f32_e32 v6, 0xc1898193, v6
	v_med3_f32 v12, v12, s71, v223
	v_exp_f32_e32 v10, v6
	v_mul_f32_e32 v4, v4, v12
	v_mul_f32_e32 v4, v8, v4
	v_fma_f32 v8, v98, s26, -v21
	v_med3_f32 v8, v8, s71, v223
	v_mul_f32_e32 v6, v6, v8
	v_fma_f32 v8, v87, s24, -v11
	v_add_f32_e32 v10, 1.0, v10
	v_max_f32_e32 v8, 0xc1898193, v8
	v_rcp_f32_e32 v10, v10
	v_fma_f32 v12, v83, s24, -v9
	v_exp_f32_e32 v14, v8
	v_max_f32_e32 v12, 0xc1898193, v12
	v_exp_f32_e32 v16, v12
	v_mul_f32_e32 v6, v10, v6
	v_add_f32_e32 v10, 1.0, v14
	v_rcp_f32_e32 v10, v10
	v_add_f32_e32 v14, 1.0, v16
	v_fma_f32 v16, v95, s26, -v15
	v_med3_f32 v16, v16, s71, v223
	v_mul_f32_e32 v8, v8, v16
	v_mul_f32_e32 v8, v10, v8
	v_fma_f32 v10, v99, s26, -v13
	v_med3_f32 v10, v10, s71, v223
	v_mul_f32_e32 v10, v12, v10
	v_fma_f32 v12, v88, s24, -v7
	v_max_f32_e32 v12, 0xc1898193, v12
	v_rcp_f32_e32 v14, v14
	v_fma_f32 v16, v84, s24, -v5
	v_exp_f32_e32 v18, v12
	v_max_f32_e32 v16, 0xc1898193, v16
	v_exp_f32_e32 v20, v16
	v_mul_f32_e32 v10, v14, v10
	v_add_f32_e32 v14, 1.0, v18
	v_rcp_f32_e32 v14, v14
	v_add_f32_e32 v18, 1.0, v20
	v_fma_f32 v20, v96, s26, -v25
	v_med3_f32 v20, v20, s71, v223
	v_mul_f32_e32 v12, v12, v20
	v_mul_f32_e32 v12, v14, v12
	v_fma_f32 v14, v100, s26, -v27
	v_med3_f32 v14, v14, s71, v223
	v_mul_f32_e32 v14, v16, v14
	v_fma_f32 v16, v89, s24, -v29
	v_max_f32_e32 v16, 0xc1898193, v16
	v_rcp_f32_e32 v18, v18
	v_fma_f32 v20, v85, s24, -v31
	v_exp_f32_e32 v22, v16
	v_max_f32_e32 v20, 0xc1898193, v20
	v_exp_f32_e32 v24, v20
	s_mov_b32 s2, 0x20000
	v_add_co_u32_e32 v40, vcc, s2, v2
	v_mul_f32_e32 v14, v18, v14
	v_add_f32_e32 v18, 1.0, v22
	v_permlane16_swap_b32_e32 v36, v38
	v_permlane16_swap_b32_e32 v37, v39
	v_addc_co_u32_e32 v41, vcc, 0, v3, vcc
	v_rcp_f32_e32 v18, v18
	global_store_dwordx4 v[40:41], v[36:39], off
	v_add_f32_e32 v22, 1.0, v24
	v_fma_f32 v24, v97, s26, -v33
	v_mov_b32_e32 v36, v199
	v_mov_b32_e32 v37, v199
	v_med3_f32 v24, v24, s71, v223
	v_cvt_pk_fp8_f32 v36, v4, v8
	v_cvt_pk_fp8_f32 v37, v6, v10
	v_fma_f32 v6, v70, s24, -v19
	v_rcp_f32_e32 v22, v22
	v_mul_f32_e32 v16, v16, v24
	v_max_f32_e32 v6, 0xc1898193, v6
	v_mul_f32_e32 v16, v18, v16
	v_fma_f32 v18, v101, s26, -v35
	v_fma_f32 v8, v66, s24, -v17
	v_exp_f32_e32 v10, v6
	v_med3_f32 v4, v18, s71, v223
	v_max_f32_e32 v8, 0xc1898193, v8
	v_mul_f32_e32 v4, v20, v4
	v_cvt_pk_fp8_f32 v36, v12, v16 op_sel:[0,0,1]
	v_exp_f32_e32 v12, v8
	v_mul_f32_e32 v4, v22, v4
	v_cvt_pk_fp8_f32 v37, v14, v4 op_sel:[0,0,1]
	v_add_f32_e32 v4, 1.0, v10
	v_rcp_f32_e32 v4, v4
	v_add_f32_e32 v10, 1.0, v12
	v_fma_f32 v12, v74, s26, -v23
	v_med3_f32 v12, v12, s71, v223
	v_mul_f32_e32 v6, v6, v12
	v_mul_f32_e32 v4, v4, v6
	v_fma_f32 v6, v78, s26, -v21
	v_med3_f32 v6, v6, s71, v223
	v_mul_f32_e32 v6, v8, v6
	v_fma_f32 v8, v71, s24, -v11
	v_max_f32_e32 v8, 0xc1898193, v8
	v_rcp_f32_e32 v10, v10
	v_fma_f32 v9, v67, s24, -v9
	v_exp_f32_e32 v11, v8
	v_max_f32_e32 v9, 0xc1898193, v9
	v_exp_f32_e32 v12, v9
	v_mul_f32_e32 v6, v10, v6
	v_add_f32_e32 v10, 1.0, v11
	v_rcp_f32_e32 v10, v10
	v_add_f32_e32 v11, 1.0, v12
	v_fma_f32 v12, v75, s26, -v15
	v_med3_f32 v12, v12, s71, v223
	v_mul_f32_e32 v8, v8, v12
	v_mul_f32_e32 v8, v10, v8
	v_fma_f32 v10, v79, s26, -v13
	v_fma_f32 v7, v72, s24, -v7
	v_med3_f32 v10, v10, s71, v223
	v_max_f32_e32 v7, 0xc1898193, v7
	v_mul_f32_e32 v9, v9, v10
	v_fma_f32 v5, v68, s24, -v5
	v_exp_f32_e32 v10, v7
	v_max_f32_e32 v5, 0xc1898193, v5
	v_rcp_f32_e32 v11, v11
	v_exp_f32_e32 v12, v5
	v_add_f32_e32 v10, 1.0, v10
	v_rcp_f32_e32 v10, v10
	v_mul_f32_e32 v9, v11, v9
	v_add_f32_e32 v11, 1.0, v12
	v_fma_f32 v12, v76, s26, -v25
	v_med3_f32 v12, v12, s71, v223
	v_mul_f32_e32 v7, v7, v12
	v_mul_f32_e32 v7, v10, v7
	v_fma_f32 v10, v80, s26, -v27
	v_med3_f32 v10, v10, s71, v223
	v_mul_f32_e32 v5, v5, v10
	v_fma_f32 v10, v73, s24, -v29
	v_max_f32_e32 v10, 0xc1898193, v10
	v_rcp_f32_e32 v11, v11
	v_fma_f32 v12, v69, s24, -v31
	v_exp_f32_e32 v13, v10
	v_max_f32_e32 v12, 0xc1898193, v12
	v_exp_f32_e32 v14, v12
	v_mul_f32_e32 v5, v11, v5
	v_add_f32_e32 v11, 1.0, v13
	v_rcp_f32_e32 v11, v11
	v_add_f32_e32 v13, 1.0, v14
	v_fma_f32 v14, v77, s26, -v33
	v_med3_f32 v14, v14, s71, v223
	v_rcp_f32_e32 v13, v13
	v_mul_f32_e32 v10, v10, v14
	v_mov_b32_e32 v38, v199
	v_mov_b32_e32 v39, v199
	v_mul_f32_e32 v10, v11, v10
	v_fma_f32 v11, v81, s26, -v35
	v_cvt_pk_fp8_f32 v38, v4, v8
	v_cvt_pk_fp8_f32 v39, v6, v9
	v_med3_f32 v11, v11, s71, v223
	v_mul_f32_e32 v4, v12, v11
	v_mul_f32_e32 v4, v13, v4
	v_cvt_pk_fp8_f32 v38, v7, v10 op_sel:[0,0,1]
	v_cvt_pk_fp8_f32 v39, v5, v4 op_sel:[0,0,1]
	v_add_co_u32_e32 v2, vcc, 0x28000, v2
	v_permlane16_swap_b32_e32 v36, v38
	s_nop 0
	v_addc_co_u32_e32 v3, vcc, 0, v3, vcc
	v_permlane16_swap_b32_e32 v37, v39
	s_and_b64 vcc, exec, s[4:5]
	s_mov_b64 s[4:5], -1
	global_store_dwordx4 v[2:3], v[36:39], off
	s_cbranch_vccnz .LBB0_975
	s_andn2_b64 vcc, exec, s[16:17]
	s_cbranch_vccnz .LBB0_974
	s_barrier
	s_branch .LBB0_974

.LBB0_1076:
	s_andn2_b64 vcc, exec, s[0:1]
	s_mov_b32 s84, s56
	s_mov_b32 s27, s68
	s_mov_b32 s56, s26
	s_mov_b32 s68, s25
	s_mov_b64 s[50:51], s[12:13]
	s_mov_b64 s[0:1], s[10:11]
	s_cbranch_vccz .LBB0_1093
	s_mov_b32 s25, s98
	s_mov_b32 s26, s99
	s_mov_b64 s[10:11], s[100:101]
	s_not_b64 s[2:3], s[0:1]
	s_branch .LBB0_1080

.LBB0_1090:
	v_lshl_add_u32 v2, s27, 8, v215
	v_ashrrev_i32_e32 v3, 31, v2
	s_ashr_i32 s0, s84, 2
	s_lshl_b32 s1, s84, 8
	v_lshl_add_u64 v[4:5], v[2:3], 2, s[92:93]
	v_add_u32_e32 v6, 0x80, v2
	v_add_u32_e32 v8, 0x90, v2
	v_add_u32_e32 v10, 0xa0, v2
	v_add_u32_e32 v2, 0xb0, v2
	s_and_b32 s84, s1, 0x300
	v_ashrrev_i32_e32 v3, 31, v2
	s_ashr_i32 s1, s0, 31
	v_readlane_b32 s40, v239, 7
	s_waitcnt vmcnt(0)
	v_ashrrev_i32_e32 v7, 31, v6
	v_ashrrev_i32_e32 v9, 31, v8
	v_ashrrev_i32_e32 v11, 31, v10
	v_lshl_add_u64 v[2:3], v[2:3], 2, s[92:93]
	s_lshl_b64 s[0:1], s[0:1], 12
	v_readlane_b32 s50, v239, 17
	v_lshl_add_u64 v[6:7], v[6:7], 2, s[92:93]
	v_lshl_add_u64 v[8:9], v[8:9], 2, s[92:93]
	v_lshl_add_u64 v[10:11], v[10:11], 2, s[92:93]
	global_load_dword v34, v[4:5], off
	global_load_dword v36, v[4:5], off offset:64
	global_load_dword v38, v[4:5], off offset:128
	global_load_dword v26, v[4:5], off offset:192
	global_load_dword v24, v[6:7], off
	global_load_dword v22, v[8:9], off
	global_load_dword v20, v[10:11], off
	global_load_dword v18, v[2:3], off
	v_or_b32_e32 v2, s84, v217
	v_readlane_b32 s51, v239, 18
	s_add_u32 s0, s50, s0
	s_addc_u32 s1, s51, s1
	v_lshlrev_b32_e32 v2, 2, v2
	global_load_dwordx4 v[14:17], v2, s[0:1]
	global_load_dwordx4 v[10:13], v2, s[0:1] offset:16
	global_load_dwordx4 v[6:9], v2, s[0:1] offset:128
	s_nop 0
	global_load_dwordx4 v[2:5], v2, s[0:1] offset:144
	s_mov_b64 s[100:101], 0
	s_and_b64 vcc, exec, s[10:11]
	s_cbranch_vccz .Lhh8_done
	s_add_i32 s40, s24, 3
	s_mul_i32 s42, s40, s72
	s_add_i32 s42, s42, s33
	s_cmp_ge_i32 s42, s83
	s_cbranch_scc1 .Lhh8_done
	s_ashr_i32 s40, s42, 31
	s_lshr_b32 s40, s40, 27
	s_add_i32 s40, s42, s40
	s_ashr_i32 s41, s40, 5
	s_lshl_b32 s41, s41, 3
	s_sub_i32 s43, s9, s41
	s_min_i32 s43, s43, 8
	s_abs_i32 s98, s43
	v_cvt_f32_u32_e32 v244, s98
	s_sub_i32 s45, 0, s98
	s_andn2_b32 s40, s40, 31
	s_sub_i32 s40, s42, s40
	v_rcp_iflag_f32_e32 v244, v244
	s_abs_i32 s42, s40
	s_xor_b32 s99, s40, s43
	s_add_i32 s41, s41, s88
	v_mul_f32_e32 v244, 0x4f7ffffe, v244
	v_cvt_u32_f32_e32 v244, v244
	s_ashr_i32 s99, s99, 31
	v_readfirstlane_b32 s46, v244
	s_mul_i32 s45, s45, s46
	s_mul_hi_u32 s45, s46, s45
	s_add_i32 s46, s46, s45
	s_mul_hi_u32 s45, s42, s46
	s_mul_i32 s46, s45, s98
	s_sub_i32 s42, s42, s46
	s_add_i32 s47, s45, 1
	s_sub_i32 s46, s42, s98
	s_cmp_ge_u32 s42, s98
	s_cselect_b32 s45, s47, s45
	s_cselect_b32 s42, s46, s42
	s_add_i32 s46, s45, 1
	s_cmp_ge_u32 s42, s98
	s_cselect_b32 s42, s46, s45
	s_xor_b32 s42, s42, s99
	s_sub_i32 s42, s42, s99
	s_mul_i32 s43, s42, s43
	s_sub_i32 s40, s40, s43
	s_add_i32 s98, s41, s40
	s_lshl_b32 s40, s98, 2
	s_add_i32 s40, s40, 0
	s_add_i32 s40, s40, 0x21400
	v_mov_b32_e32 v244, s40
	ds_read_b32 v244, v244
	s_waitcnt lgkmcnt(0)
	v_readfirstlane_b32 s40, v244
	s_lshl_b32 s40, s40, 2
	s_add_i32 s99, s40, s42
	s_mov_b64 s[100:101], -1
.Lhh8_done:
	v_mov_b32_e32 v28, v199
	v_mov_b32_e32 v29, v199
	v_mov_b32_e32 v30, v199
	v_mov_b32_e32 v31, v199
	v_mov_b32_e32 v32, v199
	v_mov_b32_e32 v33, v199
	v_readlane_b32 s41, v239, 8
	v_readlane_b32 s42, v239, 9
	v_readlane_b32 s43, v239, 10
	v_readlane_b32 s44, v239, 11
	v_readlane_b32 s45, v239, 12
	v_readlane_b32 s46, v239, 13
	v_readlane_b32 s47, v239, 14
	v_readlane_b32 s48, v239, 15
	v_readlane_b32 s49, v239, 16
	v_readlane_b32 s52, v239, 19
	v_readlane_b32 s53, v239, 20
	v_readlane_b32 s54, v239, 21
	v_readlane_b32 s55, v239, 22
	s_waitcnt vmcnt(0)
	v_ashrrev_i32_e32 v35, 31, v34
	v_lshlrev_b64 v[40:41], 10, v[34:35]
	v_cmp_lt_i64_e32 vcc, -1, v[34:35]
	v_ashrrev_i32_e32 v37, 31, v36
	v_lshlrev_b64 v[42:43], 10, v[36:37]
	v_cndmask_b32_e32 v35, 0, v41, vcc
	v_cndmask_b32_e32 v34, v221, v40, vcc
	v_cmp_lt_i64_e64 s[0:1], -1, v[36:37]
	v_lshl_add_u64 v[34:35], s[94:95], 0, v[34:35]
	v_lshl_add_u64 v[34:35], v[34:35], 0, s[84:85]
	v_pk_fma_f32 v[40:41], v[190:191], s[8:9], v[14:15] op_sel_hi:[1,0,1]
	v_pk_fma_f32 v[46:47], v[186:187], s[8:9], v[10:11] op_sel_hi:[1,0,1]
	v_pk_fma_f32 v[50:51], v[174:175], s[8:9], v[6:7] op_sel_hi:[1,0,1]
	v_pk_fma_f32 v[54:55], v[170:171], s[8:9], v[2:3] op_sel_hi:[1,0,1]
	v_cvt_pk_fp8_f32 v28, v40, v41
	v_cvt_pk_fp8_f32 v29, v46, v47
	v_cvt_pk_fp8_f32 v30, v50, v51
	v_cvt_pk_fp8_f32 v31, v54, v55
	v_pk_fma_f32 v[36:37], v[192:193], s[8:9], v[16:17] op_sel_hi:[1,0,1]
	v_pk_fma_f32 v[44:45], v[188:189], s[8:9], v[12:13] op_sel_hi:[1,0,1]
	v_pk_fma_f32 v[48:49], v[176:177], s[8:9], v[8:9] op_sel_hi:[1,0,1]
	v_pk_fma_f32 v[52:53], v[172:173], s[8:9], v[4:5] op_sel_hi:[1,0,1]
	v_cvt_pk_fp8_f32 v28, v36, v37 op_sel:[0,0,1]
	v_cvt_pk_fp8_f32 v29, v44, v45 op_sel:[0,0,1]
	v_cvt_pk_fp8_f32 v30, v48, v49 op_sel:[0,0,1]
	v_cvt_pk_fp8_f32 v31, v52, v53 op_sel:[0,0,1]
	v_lshl_add_u64 v[34:35], v[34:35], 0, s[6:7]
	v_lshl_add_u64 v[34:35], v[34:35], 0, v[202:203]
	v_permlane16_swap_b32_e32 v28, v30
	v_permlane16_swap_b32_e32 v29, v31
	v_pk_fma_f32 v[58:59], v[182:183], s[8:9], v[14:15] op_sel_hi:[1,0,1]
	v_pk_fma_f32 v[62:63], v[178:179], s[8:9], v[10:11] op_sel_hi:[1,0,1]
	global_store_dwordx4 v[34:35], v[28:31], off
	v_mov_b32_e32 v34, v199
	v_mov_b32_e32 v35, v199
	v_pk_fma_f32 v[28:29], v[166:167], s[8:9], v[6:7] op_sel_hi:[1,0,1]
	v_pk_fma_f32 v[30:31], v[162:163], s[8:9], v[2:3] op_sel_hi:[1,0,1]
	v_cvt_pk_fp8_f32 v32, v58, v59
	v_cvt_pk_fp8_f32 v33, v62, v63
	v_cvt_pk_fp8_f32 v34, v28, v29
	v_cvt_pk_fp8_f32 v35, v30, v31
	v_pk_fma_f32 v[56:57], v[184:185], s[8:9], v[16:17] op_sel_hi:[1,0,1]
	v_pk_fma_f32 v[60:61], v[180:181], s[8:9], v[12:13] op_sel_hi:[1,0,1]
	v_pk_fma_f32 v[28:29], v[168:169], s[8:9], v[8:9] op_sel_hi:[1,0,1]
	v_pk_fma_f32 v[30:31], v[164:165], s[8:9], v[4:5] op_sel_hi:[1,0,1]
	v_cndmask_b32_e64 v43, 0, v43, s[0:1]
	v_cndmask_b32_e64 v42, v221, v42, s[0:1]
	v_cvt_pk_fp8_f32 v32, v56, v57 op_sel:[0,0,1]
	v_cvt_pk_fp8_f32 v33, v60, v61 op_sel:[0,0,1]
	v_cvt_pk_fp8_f32 v34, v28, v29 op_sel:[0,0,1]
	v_cvt_pk_fp8_f32 v35, v30, v31 op_sel:[0,0,1]
	v_lshl_add_u64 v[40:41], s[94:95], 0, v[42:43]
	v_lshl_add_u64 v[40:41], v[40:41], 0, s[84:85]
	v_lshl_add_u64 v[40:41], v[40:41], 0, s[6:7]
	v_ashrrev_i32_e32 v39, 31, v38
	v_lshl_add_u64 v[28:29], v[40:41], 0, v[202:203]
	v_permlane16_swap_b32_e32 v32, v34
	v_permlane16_swap_b32_e32 v33, v35
	global_store_dwordx4 v[28:29], v[32:35], off
	v_lshlrev_b64 v[28:29], 10, v[38:39]
	v_cmp_lt_i64_e32 vcc, -1, v[38:39]
	v_pk_fma_f32 v[30:31], v[158:159], s[8:9], v[14:15] op_sel_hi:[1,0,1]
	v_pk_fma_f32 v[34:35], v[154:155], s[8:9], v[10:11] op_sel_hi:[1,0,1]
	v_cndmask_b32_e32 v29, 0, v29, vcc
	v_cndmask_b32_e32 v28, v221, v28, vcc
	v_lshl_add_u64 v[28:29], s[94:95], 0, v[28:29]
	v_lshl_add_u64 v[28:29], v[28:29], 0, s[84:85]
	v_lshl_add_u64 v[32:33], v[28:29], 0, s[6:7]
	v_mov_b32_e32 v28, v199
	v_mov_b32_e32 v29, v199
	v_cvt_pk_fp8_f32 v28, v30, v31
	v_cvt_pk_fp8_f32 v29, v34, v35
	v_pk_fma_f32 v[30:31], v[160:161], s[8:9], v[16:17] op_sel_hi:[1,0,1]
	v_pk_fma_f32 v[34:35], v[156:157], s[8:9], v[12:13] op_sel_hi:[1,0,1]
	v_cvt_pk_fp8_f32 v28, v30, v31 op_sel:[0,0,1]
	v_cvt_pk_fp8_f32 v29, v34, v35 op_sel:[0,0,1]
	v_pk_fma_f32 v[34:35], v[150:151], s[8:9], v[6:7] op_sel_hi:[1,0,1]
	v_pk_fma_f32 v[36:37], v[146:147], s[8:9], v[2:3] op_sel_hi:[1,0,1]
	v_mov_b32_e32 v30, v199
	v_mov_b32_e32 v31, v199
	v_cvt_pk_fp8_f32 v30, v34, v35
	v_cvt_pk_fp8_f32 v31, v36, v37
	v_pk_fma_f32 v[34:35], v[152:153], s[8:9], v[8:9] op_sel_hi:[1,0,1]
	v_pk_fma_f32 v[36:37], v[148:149], s[8:9], v[4:5] op_sel_hi:[1,0,1]
	v_cvt_pk_fp8_f32 v30, v34, v35 op_sel:[0,0,1]
	v_cvt_pk_fp8_f32 v31, v36, v37 op_sel:[0,0,1]
	v_ashrrev_i32_e32 v27, 31, v26
	v_lshl_add_u64 v[32:33], v[32:33], 0, v[202:203]
	v_permlane16_swap_b32_e32 v28, v30
	v_permlane16_swap_b32_e32 v29, v31
	global_store_dwordx4 v[32:33], v[28:31], off
	v_cmp_lt_i64_e32 vcc, -1, v[26:27]
	v_pk_fma_f32 v[32:33], v[138:139], s[8:9], v[10:11] op_sel_hi:[1,0,1]
	v_lshlrev_b64 v[28:29], 10, v[26:27]
	v_cndmask_b32_e32 v27, 0, v29, vcc
	v_cndmask_b32_e32 v26, v221, v28, vcc
	v_lshl_add_u64 v[26:27], s[94:95], 0, v[26:27]
	v_lshl_add_u64 v[26:27], v[26:27], 0, s[84:85]
	v_lshl_add_u64 v[30:31], v[26:27], 0, s[6:7]
	v_pk_fma_f32 v[28:29], v[142:143], s[8:9], v[14:15] op_sel_hi:[1,0,1]
	v_mov_b32_e32 v26, v199
	v_mov_b32_e32 v27, v199
	v_cvt_pk_fp8_f32 v26, v28, v29
	v_cvt_pk_fp8_f32 v27, v32, v33
	v_pk_fma_f32 v[28:29], v[144:145], s[8:9], v[16:17] op_sel_hi:[1,0,1]
	v_pk_fma_f32 v[32:33], v[140:141], s[8:9], v[12:13] op_sel_hi:[1,0,1]
	v_cvt_pk_fp8_f32 v26, v28, v29 op_sel:[0,0,1]
	v_cvt_pk_fp8_f32 v27, v32, v33 op_sel:[0,0,1]
	v_pk_fma_f32 v[32:33], v[134:135], s[8:9], v[6:7] op_sel_hi:[1,0,1]
	v_pk_fma_f32 v[34:35], v[130:131], s[8:9], v[2:3] op_sel_hi:[1,0,1]
	v_mov_b32_e32 v28, v199
	v_mov_b32_e32 v29, v199
	v_cvt_pk_fp8_f32 v28, v32, v33
	v_cvt_pk_fp8_f32 v29, v34, v35
	v_pk_fma_f32 v[32:33], v[136:137], s[8:9], v[8:9] op_sel_hi:[1,0,1]
	v_pk_fma_f32 v[34:35], v[132:133], s[8:9], v[4:5] op_sel_hi:[1,0,1]
	v_cvt_pk_fp8_f32 v28, v32, v33 op_sel:[0,0,1]
	v_cvt_pk_fp8_f32 v29, v34, v35 op_sel:[0,0,1]
	v_ashrrev_i32_e32 v25, 31, v24
	v_lshl_add_u64 v[30:31], v[30:31], 0, v[202:203]
	v_permlane16_swap_b32_e32 v26, v28
	v_permlane16_swap_b32_e32 v27, v29
	global_store_dwordx4 v[30:31], v[26:29], off
	v_cmp_lt_i64_e32 vcc, -1, v[24:25]
	v_pk_fma_f32 v[30:31], v[122:123], s[8:9], v[10:11] op_sel_hi:[1,0,1]
	v_lshlrev_b64 v[26:27], 10, v[24:25]
	v_cndmask_b32_e32 v25, 0, v27, vcc
	v_cndmask_b32_e32 v24, v221, v26, vcc
	v_lshl_add_u64 v[24:25], s[94:95], 0, v[24:25]
	v_lshl_add_u64 v[24:25], v[24:25], 0, s[84:85]
	v_lshl_add_u64 v[28:29], v[24:25], 0, s[6:7]
	v_pk_fma_f32 v[26:27], v[126:127], s[8:9], v[14:15] op_sel_hi:[1,0,1]
	v_mov_b32_e32 v24, v199
	v_mov_b32_e32 v25, v199
	v_cvt_pk_fp8_f32 v24, v26, v27
	v_cvt_pk_fp8_f32 v25, v30, v31
	v_pk_fma_f32 v[26:27], v[128:129], s[8:9], v[16:17] op_sel_hi:[1,0,1]
	v_pk_fma_f32 v[30:31], v[124:125], s[8:9], v[12:13] op_sel_hi:[1,0,1]
	v_cvt_pk_fp8_f32 v24, v26, v27 op_sel:[0,0,1]
	v_cvt_pk_fp8_f32 v25, v30, v31 op_sel:[0,0,1]
	v_pk_fma_f32 v[30:31], v[118:119], s[8:9], v[6:7] op_sel_hi:[1,0,1]
	v_pk_fma_f32 v[32:33], v[114:115], s[8:9], v[2:3] op_sel_hi:[1,0,1]
	v_mov_b32_e32 v26, v199
	v_mov_b32_e32 v27, v199
	v_cvt_pk_fp8_f32 v26, v30, v31
	v_cvt_pk_fp8_f32 v27, v32, v33
	v_pk_fma_f32 v[30:31], v[120:121], s[8:9], v[8:9] op_sel_hi:[1,0,1]
	v_pk_fma_f32 v[32:33], v[116:117], s[8:9], v[4:5] op_sel_hi:[1,0,1]
	v_cvt_pk_fp8_f32 v26, v30, v31 op_sel:[0,0,1]
	v_cvt_pk_fp8_f32 v27, v32, v33 op_sel:[0,0,1]
	v_ashrrev_i32_e32 v23, 31, v22
	v_lshl_add_u64 v[28:29], v[28:29], 0, v[202:203]
	v_permlane16_swap_b32_e32 v24, v26
	v_permlane16_swap_b32_e32 v25, v27
	global_store_dwordx4 v[28:29], v[24:27], off
	v_cmp_lt_i64_e32 vcc, -1, v[22:23]
	v_pk_fma_f32 v[28:29], v[98:99], s[8:9], v[10:11] op_sel_hi:[1,0,1]
	v_lshlrev_b64 v[24:25], 10, v[22:23]
	v_cndmask_b32_e32 v23, 0, v25, vcc
	v_cndmask_b32_e32 v22, v221, v24, vcc
	v_lshl_add_u64 v[22:23], s[94:95], 0, v[22:23]
	v_lshl_add_u64 v[22:23], v[22:23], 0, s[84:85]
	v_lshl_add_u64 v[26:27], v[22:23], 0, s[6:7]
	v_pk_fma_f32 v[24:25], v[106:107], s[8:9], v[14:15] op_sel_hi:[1,0,1]
	v_mov_b32_e32 v22, v199
	v_mov_b32_e32 v23, v199
	v_cvt_pk_fp8_f32 v22, v24, v25
	v_cvt_pk_fp8_f32 v23, v28, v29
	v_pk_fma_f32 v[24:25], v[108:109], s[8:9], v[16:17] op_sel_hi:[1,0,1]
	v_pk_fma_f32 v[28:29], v[100:101], s[8:9], v[12:13] op_sel_hi:[1,0,1]
	v_cvt_pk_fp8_f32 v22, v24, v25 op_sel:[0,0,1]
	v_cvt_pk_fp8_f32 v23, v28, v29 op_sel:[0,0,1]
	v_pk_fma_f32 v[28:29], v[90:91], s[8:9], v[6:7] op_sel_hi:[1,0,1]
	v_pk_fma_f32 v[30:31], v[82:83], s[8:9], v[2:3] op_sel_hi:[1,0,1]
	v_mov_b32_e32 v24, v199
	v_mov_b32_e32 v25, v199
	v_cvt_pk_fp8_f32 v24, v28, v29
	v_cvt_pk_fp8_f32 v25, v30, v31
	v_pk_fma_f32 v[28:29], v[92:93], s[8:9], v[8:9] op_sel_hi:[1,0,1]
	v_pk_fma_f32 v[30:31], v[84:85], s[8:9], v[4:5] op_sel_hi:[1,0,1]
	v_cvt_pk_fp8_f32 v24, v28, v29 op_sel:[0,0,1]
	v_cvt_pk_fp8_f32 v25, v30, v31 op_sel:[0,0,1]
	v_ashrrev_i32_e32 v21, 31, v20
	v_lshl_add_u64 v[26:27], v[26:27], 0, v[202:203]
	v_permlane16_swap_b32_e32 v22, v24
	v_permlane16_swap_b32_e32 v23, v25
	global_store_dwordx4 v[26:27], v[22:25], off
	v_cmp_lt_i64_e32 vcc, -1, v[20:21]
	v_pk_fma_f32 v[26:27], v[74:75], s[8:9], v[10:11] op_sel_hi:[1,0,1]
	v_lshlrev_b64 v[22:23], 10, v[20:21]
	v_cndmask_b32_e32 v21, 0, v23, vcc
	v_cndmask_b32_e32 v20, v221, v22, vcc
	v_lshl_add_u64 v[20:21], s[94:95], 0, v[20:21]
	v_lshl_add_u64 v[20:21], v[20:21], 0, s[84:85]
	v_lshl_add_u64 v[24:25], v[20:21], 0, s[6:7]
	v_pk_fma_f32 v[22:23], v[78:79], s[8:9], v[14:15] op_sel_hi:[1,0,1]
	v_mov_b32_e32 v20, v199
	v_mov_b32_e32 v21, v199
	v_cvt_pk_fp8_f32 v20, v22, v23
	v_cvt_pk_fp8_f32 v21, v26, v27
	v_pk_fma_f32 v[22:23], v[80:81], s[8:9], v[16:17] op_sel_hi:[1,0,1]
	v_pk_fma_f32 v[26:27], v[76:77], s[8:9], v[12:13] op_sel_hi:[1,0,1]
	v_cvt_pk_fp8_f32 v20, v22, v23 op_sel:[0,0,1]
	v_cvt_pk_fp8_f32 v21, v26, v27 op_sel:[0,0,1]
	v_pk_fma_f32 v[26:27], v[102:103], s[8:9], v[6:7] op_sel_hi:[1,0,1]
	v_pk_fma_f32 v[28:29], v[110:111], s[8:9], v[2:3] op_sel_hi:[1,0,1]
	v_mov_b32_e32 v22, v199
	v_mov_b32_e32 v23, v199
	v_cvt_pk_fp8_f32 v22, v26, v27
	v_cvt_pk_fp8_f32 v23, v28, v29
	v_pk_fma_f32 v[26:27], v[104:105], s[8:9], v[8:9] op_sel_hi:[1,0,1]
	v_pk_fma_f32 v[28:29], v[112:113], s[8:9], v[4:5] op_sel_hi:[1,0,1]
	v_cvt_pk_fp8_f32 v22, v26, v27 op_sel:[0,0,1]
	v_cvt_pk_fp8_f32 v23, v28, v29 op_sel:[0,0,1]
	v_ashrrev_i32_e32 v19, 31, v18
	v_lshl_add_u64 v[24:25], v[24:25], 0, v[202:203]
	v_permlane16_swap_b32_e32 v20, v22
	v_permlane16_swap_b32_e32 v21, v23
	global_store_dwordx4 v[24:25], v[20:23], off
	v_cmp_lt_i64_e32 vcc, -1, v[18:19]
	v_pk_fma_f32 v[12:13], v[68:69], s[8:9], v[12:13] op_sel_hi:[1,0,1]
	v_lshlrev_b64 v[20:21], 10, v[18:19]
	v_cndmask_b32_e32 v19, 0, v21, vcc
	v_cndmask_b32_e32 v18, v221, v20, vcc
	v_pk_fma_f32 v[20:21], v[66:67], s[8:9], v[10:11] op_sel_hi:[1,0,1]
	v_mov_b32_e32 v11, v199
	v_cvt_pk_fp8_f32 v11, v20, v21
	v_pk_fma_f32 v[14:15], v[70:71], s[8:9], v[14:15] op_sel_hi:[1,0,1]
	v_mov_b32_e32 v10, v199
	v_pk_fma_f32 v[6:7], v[86:87], s[8:9], v[6:7] op_sel_hi:[1,0,1]
	v_cvt_pk_fp8_f32 v11, v12, v13 op_sel:[0,0,1]
	v_pk_fma_f32 v[2:3], v[94:95], s[8:9], v[2:3] op_sel_hi:[1,0,1]
	v_mov_b32_e32 v12, v199
	v_mov_b32_e32 v13, v199
	v_cvt_pk_fp8_f32 v10, v14, v15
	v_cvt_pk_fp8_f32 v12, v6, v7
	v_cvt_pk_fp8_f32 v13, v2, v3
	v_pk_fma_f32 v[14:15], v[72:73], s[8:9], v[16:17] op_sel_hi:[1,0,1]
	v_pk_fma_f32 v[2:3], v[88:89], s[8:9], v[8:9] op_sel_hi:[1,0,1]
	v_pk_fma_f32 v[4:5], v[96:97], s[8:9], v[4:5] op_sel_hi:[1,0,1]
	v_cvt_pk_fp8_f32 v10, v14, v15 op_sel:[0,0,1]
	v_cvt_pk_fp8_f32 v12, v2, v3 op_sel:[0,0,1]
	v_cvt_pk_fp8_f32 v13, v4, v5 op_sel:[0,0,1]
	v_lshl_add_u64 v[18:19], s[94:95], 0, v[18:19]
	v_lshl_add_u64 v[18:19], v[18:19], 0, s[84:85]
	v_lshl_add_u64 v[18:19], v[18:19], 0, s[6:7]
	v_lshl_add_u64 v[2:3], v[18:19], 0, v[202:203]
	v_permlane16_swap_b32_e32 v10, v12
	v_permlane16_swap_b32_e32 v11, v13
	s_and_b64 vcc, exec, s[2:3]
	s_mov_b64 s[0:1], -1
	global_store_dwordx4 v[2:3], v[10:13], off
	s_cbranch_vccnz .LBB0_1076
	s_andn2_b64 vcc, exec, s[90:91]
	s_cbranch_vccnz .LBB0_1075
	s_barrier
	s_branch .LBB0_1075
